# attention sub-tiles: deferred-max test on each lane half's own row maximum; the cross-half permlane swap max only in the rescale path
# speedup vs baseline: 1.0128x; 1.0107x over previous
.LBB0_452:
	s_nop 0
	v_max3_f32 v2, v70, v71, v72
	v_max3_f32 v4, v73, v74, v75
	v_max3_f32 v5, v76, v77, v78
	v_max3_f32 v175, v79, v80, v81
	v_max3_f32 v2, v2, v4, v5
	v_max3_f32 v4, v82, v83, v84
	v_max3_f32 v2, v2, v175, v4
	v_max_f32_e32 v2, v2, v85
	v_sub_f32_e32 v4, v2, v168
	v_cmp_ge_f32_e32 vcc, s76, v4
	s_cmp_eq_u64 vcc, exec
	s_cbranch_scc1 .LBB0_454
	v_mov_b32_e32 v4, v2
	s_nop 1
	v_permlane32_swap_b32_e32 v2, v4
	v_max_f32_e32 v2, v2, v4
	v_max_f32_e32 v2, v2, v2
	v_max_f32_e32 v4, v168, v168
	v_max_f32_e32 v4, v4, v2
	v_sub_f32_e32 v2, v168, v4
	v_mul_f32_e32 v2, 0x3fb8aa3b, v2
	v_exp_f32_e32 v2, v2
	v_mov_b32_e32 v168, v4
	v_mul_f32_e32 v167, v167, v2
	v_pk_mul_f32 v[68:69], v[68:69], v[2:3] op_sel_hi:[1,0]
	v_pk_mul_f32 v[66:67], v[66:67], v[2:3] op_sel_hi:[1,0]
	v_pk_mul_f32 v[64:65], v[64:65], v[2:3] op_sel_hi:[1,0]
	v_pk_mul_f32 v[62:63], v[62:63], v[2:3] op_sel_hi:[1,0]
	v_pk_mul_f32 v[60:61], v[60:61], v[2:3] op_sel_hi:[1,0]
	v_pk_mul_f32 v[58:59], v[58:59], v[2:3] op_sel_hi:[1,0]
	v_pk_mul_f32 v[56:57], v[56:57], v[2:3] op_sel_hi:[1,0]
	v_pk_mul_f32 v[54:55], v[54:55], v[2:3] op_sel_hi:[1,0]
	v_pk_mul_f32 v[52:53], v[52:53], v[2:3] op_sel_hi:[1,0]
	v_pk_mul_f32 v[50:51], v[50:51], v[2:3] op_sel_hi:[1,0]
	v_pk_mul_f32 v[48:49], v[48:49], v[2:3] op_sel_hi:[1,0]
	v_pk_mul_f32 v[46:47], v[46:47], v[2:3] op_sel_hi:[1,0]
	v_pk_mul_f32 v[44:45], v[44:45], v[2:3] op_sel_hi:[1,0]
	v_pk_mul_f32 v[42:43], v[42:43], v[2:3] op_sel_hi:[1,0]
	v_pk_mul_f32 v[40:41], v[40:41], v[2:3] op_sel_hi:[1,0]
	v_pk_mul_f32 v[38:39], v[38:39], v[2:3] op_sel_hi:[1,0]
	v_pk_mul_f32 v[36:37], v[36:37], v[2:3] op_sel_hi:[1,0]
	v_pk_mul_f32 v[34:35], v[34:35], v[2:3] op_sel_hi:[1,0]
	v_pk_mul_f32 v[32:33], v[32:33], v[2:3] op_sel_hi:[1,0]
	v_pk_mul_f32 v[30:31], v[30:31], v[2:3] op_sel_hi:[1,0]
	v_pk_mul_f32 v[28:29], v[28:29], v[2:3] op_sel_hi:[1,0]
	v_pk_mul_f32 v[26:27], v[26:27], v[2:3] op_sel_hi:[1,0]
	v_pk_mul_f32 v[24:25], v[24:25], v[2:3] op_sel_hi:[1,0]
	v_pk_mul_f32 v[22:23], v[22:23], v[2:3] op_sel_hi:[1,0]
	v_pk_mul_f32 v[20:21], v[20:21], v[2:3] op_sel_hi:[1,0]
	v_pk_mul_f32 v[18:19], v[18:19], v[2:3] op_sel_hi:[1,0]
	v_pk_mul_f32 v[16:17], v[16:17], v[2:3] op_sel_hi:[1,0]
	v_pk_mul_f32 v[14:15], v[14:15], v[2:3] op_sel_hi:[1,0]
	v_pk_mul_f32 v[12:13], v[12:13], v[2:3] op_sel_hi:[1,0]
	v_pk_mul_f32 v[10:11], v[10:11], v[2:3] op_sel_hi:[1,0]
	v_pk_mul_f32 v[8:9], v[8:9], v[2:3] op_sel_hi:[1,0]
	v_pk_mul_f32 v[6:7], v[6:7], v[2:3] op_sel_hi:[1,0]

.LBB0_458:
	s_nop 0
	v_max3_f32 v2, v70, v71, v72
	v_max3_f32 v4, v73, v74, v75
	v_max3_f32 v5, v76, v77, v78
	v_max3_f32 v169, v79, v80, v81
	v_max3_f32 v2, v2, v4, v5
	v_max3_f32 v4, v82, v83, v84
	v_max3_f32 v2, v2, v169, v4
	v_max_f32_e32 v2, v2, v85
	v_sub_f32_e32 v4, v2, v168
	v_cmp_ge_f32_e32 vcc, s76, v4
	s_cmp_eq_u64 vcc, exec
	s_cbranch_scc1 .LBB0_460
	v_mov_b32_e32 v4, v2
	s_nop 1
	v_permlane32_swap_b32_e32 v2, v4
	v_max_f32_e32 v2, v2, v4
	v_max_f32_e32 v2, v2, v2
	v_max_f32_e32 v4, v168, v168
	v_max_f32_e32 v4, v4, v2
	v_sub_f32_e32 v2, v168, v4
	v_mul_f32_e32 v2, 0x3fb8aa3b, v2
	v_exp_f32_e32 v2, v2
	v_mov_b32_e32 v168, v4
	v_mul_f32_e32 v167, v167, v2
	v_pk_mul_f32 v[68:69], v[68:69], v[2:3] op_sel_hi:[1,0]
	v_pk_mul_f32 v[66:67], v[66:67], v[2:3] op_sel_hi:[1,0]
	v_pk_mul_f32 v[64:65], v[64:65], v[2:3] op_sel_hi:[1,0]
	v_pk_mul_f32 v[62:63], v[62:63], v[2:3] op_sel_hi:[1,0]
	v_pk_mul_f32 v[60:61], v[60:61], v[2:3] op_sel_hi:[1,0]
	v_pk_mul_f32 v[58:59], v[58:59], v[2:3] op_sel_hi:[1,0]
	v_pk_mul_f32 v[56:57], v[56:57], v[2:3] op_sel_hi:[1,0]
	v_pk_mul_f32 v[54:55], v[54:55], v[2:3] op_sel_hi:[1,0]
	v_pk_mul_f32 v[52:53], v[52:53], v[2:3] op_sel_hi:[1,0]
	v_pk_mul_f32 v[50:51], v[50:51], v[2:3] op_sel_hi:[1,0]
	v_pk_mul_f32 v[48:49], v[48:49], v[2:3] op_sel_hi:[1,0]
	v_pk_mul_f32 v[46:47], v[46:47], v[2:3] op_sel_hi:[1,0]
	v_pk_mul_f32 v[44:45], v[44:45], v[2:3] op_sel_hi:[1,0]
	v_pk_mul_f32 v[42:43], v[42:43], v[2:3] op_sel_hi:[1,0]
	v_pk_mul_f32 v[40:41], v[40:41], v[2:3] op_sel_hi:[1,0]
	v_pk_mul_f32 v[38:39], v[38:39], v[2:3] op_sel_hi:[1,0]
	v_pk_mul_f32 v[36:37], v[36:37], v[2:3] op_sel_hi:[1,0]
	v_pk_mul_f32 v[34:35], v[34:35], v[2:3] op_sel_hi:[1,0]
	v_pk_mul_f32 v[32:33], v[32:33], v[2:3] op_sel_hi:[1,0]
	v_pk_mul_f32 v[30:31], v[30:31], v[2:3] op_sel_hi:[1,0]
	v_pk_mul_f32 v[28:29], v[28:29], v[2:3] op_sel_hi:[1,0]
	v_pk_mul_f32 v[26:27], v[26:27], v[2:3] op_sel_hi:[1,0]
	v_pk_mul_f32 v[24:25], v[24:25], v[2:3] op_sel_hi:[1,0]
	v_pk_mul_f32 v[22:23], v[22:23], v[2:3] op_sel_hi:[1,0]
	v_pk_mul_f32 v[20:21], v[20:21], v[2:3] op_sel_hi:[1,0]
	v_pk_mul_f32 v[18:19], v[18:19], v[2:3] op_sel_hi:[1,0]
	v_pk_mul_f32 v[16:17], v[16:17], v[2:3] op_sel_hi:[1,0]
	v_pk_mul_f32 v[14:15], v[14:15], v[2:3] op_sel_hi:[1,0]
	v_pk_mul_f32 v[12:13], v[12:13], v[2:3] op_sel_hi:[1,0]
	v_pk_mul_f32 v[10:11], v[10:11], v[2:3] op_sel_hi:[1,0]
	v_pk_mul_f32 v[8:9], v[8:9], v[2:3] op_sel_hi:[1,0]
	v_pk_mul_f32 v[6:7], v[6:7], v[2:3] op_sel_hi:[1,0]

.LBB0_524:
	s_nop 1
	v_max3_f32 v2, v50, v51, v52
	v_max3_f32 v116, v53, v54, v55
	v_max3_f32 v117, v56, v57, v58
	v_max3_f32 v118, v59, v60, v61
	v_max3_f32 v2, v2, v116, v117
	v_max3_f32 v116, v62, v63, v64
	v_max3_f32 v2, v2, v118, v116
	v_max_f32_e32 v2, v2, v65
	v_sub_f32_e32 v116, v2, v110
	v_cmp_ge_f32_e32 vcc, s76, v116
	s_cmp_eq_u64 vcc, exec
	s_cbranch_scc1 .LBB0_526
	v_mov_b32_e32 v116, v2
	s_nop 1
	v_permlane32_swap_b32_e32 v2, v116
	v_max_f32_e32 v2, v2, v116
	v_max_f32_e32 v2, v2, v2
	v_max_f32_e32 v116, v110, v110
	v_max_f32_e32 v116, v116, v2
	v_sub_f32_e32 v2, v110, v116
	v_mul_f32_e32 v2, 0x3fb8aa3b, v2
	v_exp_f32_e32 v2, v2
	v_mov_b32_e32 v110, v116
	v_mul_f32_e32 v107, v107, v2
	v_pk_mul_f32 v[48:49], v[48:49], v[2:3] op_sel_hi:[1,0]
	v_pk_mul_f32 v[46:47], v[46:47], v[2:3] op_sel_hi:[1,0]
	v_pk_mul_f32 v[44:45], v[44:45], v[2:3] op_sel_hi:[1,0]
	v_pk_mul_f32 v[42:43], v[42:43], v[2:3] op_sel_hi:[1,0]
	v_pk_mul_f32 v[40:41], v[40:41], v[2:3] op_sel_hi:[1,0]
	v_pk_mul_f32 v[38:39], v[38:39], v[2:3] op_sel_hi:[1,0]
	v_pk_mul_f32 v[36:37], v[36:37], v[2:3] op_sel_hi:[1,0]
	v_pk_mul_f32 v[34:35], v[34:35], v[2:3] op_sel_hi:[1,0]
	v_pk_mul_f32 v[32:33], v[32:33], v[2:3] op_sel_hi:[1,0]
	v_pk_mul_f32 v[30:31], v[30:31], v[2:3] op_sel_hi:[1,0]
	v_pk_mul_f32 v[28:29], v[28:29], v[2:3] op_sel_hi:[1,0]
	v_pk_mul_f32 v[26:27], v[26:27], v[2:3] op_sel_hi:[1,0]
	v_pk_mul_f32 v[24:25], v[24:25], v[2:3] op_sel_hi:[1,0]
	v_pk_mul_f32 v[22:23], v[22:23], v[2:3] op_sel_hi:[1,0]
	v_pk_mul_f32 v[20:21], v[20:21], v[2:3] op_sel_hi:[1,0]
	v_pk_mul_f32 v[18:19], v[18:19], v[2:3] op_sel_hi:[1,0]

.LBB0_530:
	s_nop 0
	v_max3_f32 v2, v50, v51, v52
	v_max3_f32 v16, v53, v54, v55
	v_max3_f32 v17, v56, v57, v58
	v_max3_f32 v111, v59, v60, v61
	v_max3_f32 v2, v2, v16, v17
	v_max3_f32 v16, v62, v63, v64
	v_max3_f32 v2, v2, v111, v16
	v_max_f32_e32 v2, v2, v65
	v_sub_f32_e32 v16, v2, v110
	v_cmp_ge_f32_e32 vcc, s76, v16
	s_cmp_eq_u64 vcc, exec
	s_cbranch_scc1 .LBB0_509
	v_mov_b32_e32 v16, v2
	s_nop 1
	v_permlane32_swap_b32_e32 v2, v16
	v_max_f32_e32 v2, v2, v16
	v_max_f32_e32 v2, v2, v2
	v_max_f32_e32 v16, v110, v110
	v_max_f32_e32 v16, v16, v2
	v_sub_f32_e32 v2, v110, v16
	v_mul_f32_e32 v2, 0x3fb8aa3b, v2
	v_exp_f32_e32 v2, v2
	v_mov_b32_e32 v110, v16
	v_mul_f32_e32 v107, v107, v2
	v_pk_mul_f32 v[48:49], v[48:49], v[2:3] op_sel_hi:[1,0]
	v_pk_mul_f32 v[46:47], v[46:47], v[2:3] op_sel_hi:[1,0]
	v_pk_mul_f32 v[44:45], v[44:45], v[2:3] op_sel_hi:[1,0]
	v_pk_mul_f32 v[42:43], v[42:43], v[2:3] op_sel_hi:[1,0]
	v_pk_mul_f32 v[40:41], v[40:41], v[2:3] op_sel_hi:[1,0]
	v_pk_mul_f32 v[38:39], v[38:39], v[2:3] op_sel_hi:[1,0]
	v_pk_mul_f32 v[36:37], v[36:37], v[2:3] op_sel_hi:[1,0]
	v_pk_mul_f32 v[34:35], v[34:35], v[2:3] op_sel_hi:[1,0]
	v_pk_mul_f32 v[32:33], v[32:33], v[2:3] op_sel_hi:[1,0]
	v_pk_mul_f32 v[30:31], v[30:31], v[2:3] op_sel_hi:[1,0]
	v_pk_mul_f32 v[28:29], v[28:29], v[2:3] op_sel_hi:[1,0]
	v_pk_mul_f32 v[26:27], v[26:27], v[2:3] op_sel_hi:[1,0]
	v_pk_mul_f32 v[24:25], v[24:25], v[2:3] op_sel_hi:[1,0]
	v_pk_mul_f32 v[22:23], v[22:23], v[2:3] op_sel_hi:[1,0]
	v_pk_mul_f32 v[20:21], v[20:21], v[2:3] op_sel_hi:[1,0]
	v_pk_mul_f32 v[18:19], v[18:19], v[2:3] op_sel_hi:[1,0]
	s_branch .LBB0_509

.LBB0_687:
	s_nop 0
	v_max3_f32 v2, v82, v83, v84
	v_max3_f32 v164, v85, v86, v87
	v_max3_f32 v165, v88, v89, v90
	v_max3_f32 v166, v91, v92, v93
	v_max3_f32 v2, v2, v164, v165
	v_max3_f32 v164, v94, v95, v96
	v_max3_f32 v2, v2, v166, v164
	v_max_f32_e32 v2, v2, v97
	v_sub_f32_e32 v164, v2, v158
	v_cmp_ge_f32_e32 vcc, s76, v164
	s_cmp_eq_u64 vcc, exec
	s_cbranch_scc1 .LBB0_689
	v_mov_b32_e32 v164, v2
	s_nop 1
	v_permlane32_swap_b32_e32 v2, v164
	v_max_f32_e32 v2, v2, v164
	v_max_f32_e32 v2, v2, v2
	v_max_f32_e32 v164, v158, v158
	v_max_f32_e32 v164, v164, v2
	v_sub_f32_e32 v2, v158, v164
	v_mul_f32_e32 v2, 0x3fb8aa3b, v2
	v_exp_f32_e32 v2, v2
	v_mov_b32_e32 v158, v164
	v_mul_f32_e32 v144, v144, v2
	v_pk_mul_f32 v[80:81], v[80:81], v[2:3] op_sel_hi:[1,0]
	v_pk_mul_f32 v[78:79], v[78:79], v[2:3] op_sel_hi:[1,0]
	v_pk_mul_f32 v[76:77], v[76:77], v[2:3] op_sel_hi:[1,0]
	v_pk_mul_f32 v[74:75], v[74:75], v[2:3] op_sel_hi:[1,0]
	v_pk_mul_f32 v[72:73], v[72:73], v[2:3] op_sel_hi:[1,0]
	v_pk_mul_f32 v[70:71], v[70:71], v[2:3] op_sel_hi:[1,0]
	v_pk_mul_f32 v[68:69], v[68:69], v[2:3] op_sel_hi:[1,0]
	v_pk_mul_f32 v[66:67], v[66:67], v[2:3] op_sel_hi:[1,0]
	v_pk_mul_f32 v[64:65], v[64:65], v[2:3] op_sel_hi:[1,0]
	v_pk_mul_f32 v[62:63], v[62:63], v[2:3] op_sel_hi:[1,0]
	v_pk_mul_f32 v[60:61], v[60:61], v[2:3] op_sel_hi:[1,0]
	v_pk_mul_f32 v[58:59], v[58:59], v[2:3] op_sel_hi:[1,0]
	v_pk_mul_f32 v[56:57], v[56:57], v[2:3] op_sel_hi:[1,0]
	v_pk_mul_f32 v[54:55], v[54:55], v[2:3] op_sel_hi:[1,0]
	v_pk_mul_f32 v[52:53], v[52:53], v[2:3] op_sel_hi:[1,0]
	v_pk_mul_f32 v[50:51], v[50:51], v[2:3] op_sel_hi:[1,0]

.LBB0_695:
	s_nop 0
	v_max3_f32 v2, v82, v83, v84
	v_max3_f32 v16, v85, v86, v87
	v_max3_f32 v17, v88, v89, v90
	v_max3_f32 v159, v91, v92, v93
	v_max3_f32 v2, v2, v16, v17
	v_max3_f32 v16, v94, v95, v96
	v_max3_f32 v2, v2, v159, v16
	v_max_f32_e32 v2, v2, v97
	v_sub_f32_e32 v16, v2, v158
	v_cmp_ge_f32_e32 vcc, s76, v16
	s_cmp_eq_u64 vcc, exec
	s_cbranch_scc1 .LBB0_668
	v_mov_b32_e32 v16, v2
	s_nop 1
	v_permlane32_swap_b32_e32 v2, v16
	v_max_f32_e32 v2, v2, v16
	v_max_f32_e32 v2, v2, v2
	v_max_f32_e32 v16, v158, v158
	v_max_f32_e32 v16, v16, v2
	v_sub_f32_e32 v2, v158, v16
	v_mul_f32_e32 v2, 0x3fb8aa3b, v2
	v_exp_f32_e32 v2, v2
	v_mov_b32_e32 v158, v16
	v_mul_f32_e32 v144, v144, v2
	v_pk_mul_f32 v[80:81], v[80:81], v[2:3] op_sel_hi:[1,0]
	v_pk_mul_f32 v[78:79], v[78:79], v[2:3] op_sel_hi:[1,0]
	v_pk_mul_f32 v[76:77], v[76:77], v[2:3] op_sel_hi:[1,0]
	v_pk_mul_f32 v[74:75], v[74:75], v[2:3] op_sel_hi:[1,0]
	v_pk_mul_f32 v[72:73], v[72:73], v[2:3] op_sel_hi:[1,0]
	v_pk_mul_f32 v[70:71], v[70:71], v[2:3] op_sel_hi:[1,0]
	v_pk_mul_f32 v[68:69], v[68:69], v[2:3] op_sel_hi:[1,0]
	v_pk_mul_f32 v[66:67], v[66:67], v[2:3] op_sel_hi:[1,0]
	v_pk_mul_f32 v[64:65], v[64:65], v[2:3] op_sel_hi:[1,0]
	v_pk_mul_f32 v[62:63], v[62:63], v[2:3] op_sel_hi:[1,0]
	v_pk_mul_f32 v[60:61], v[60:61], v[2:3] op_sel_hi:[1,0]
	v_pk_mul_f32 v[58:59], v[58:59], v[2:3] op_sel_hi:[1,0]
	v_pk_mul_f32 v[56:57], v[56:57], v[2:3] op_sel_hi:[1,0]
	v_pk_mul_f32 v[54:55], v[54:55], v[2:3] op_sel_hi:[1,0]
	v_pk_mul_f32 v[52:53], v[52:53], v[2:3] op_sel_hi:[1,0]
	v_pk_mul_f32 v[50:51], v[50:51], v[2:3] op_sel_hi:[1,0]
	s_branch .LBB0_668

.LBB0_785:
	s_nop 1
	v_max3_f32 v2, v50, v51, v52
	v_max3_f32 v119, v53, v54, v55
	v_max3_f32 v120, v56, v57, v58
	v_max3_f32 v121, v59, v60, v61
	v_max3_f32 v2, v2, v119, v120
	v_max3_f32 v119, v62, v63, v64
	v_max3_f32 v2, v2, v121, v119
	v_max_f32_e32 v2, v2, v65
	v_sub_f32_e32 v119, v2, v113
	v_cmp_ge_f32_e32 vcc, s76, v119
	s_cmp_eq_u64 vcc, exec
	s_cbranch_scc1 .LBB0_787
	v_mov_b32_e32 v119, v2
	s_nop 1
	v_permlane32_swap_b32_e32 v2, v119
	v_max_f32_e32 v2, v2, v119
	v_max_f32_e32 v2, v2, v2
	v_max_f32_e32 v119, v113, v113
	v_max_f32_e32 v119, v119, v2
	v_sub_f32_e32 v2, v113, v119
	v_mul_f32_e32 v2, 0x3fb8aa3b, v2
	v_exp_f32_e32 v2, v2
	v_mov_b32_e32 v113, v119
	v_mul_f32_e32 v108, v108, v2
	v_pk_mul_f32 v[48:49], v[48:49], v[2:3] op_sel_hi:[1,0]
	v_pk_mul_f32 v[46:47], v[46:47], v[2:3] op_sel_hi:[1,0]
	v_pk_mul_f32 v[44:45], v[44:45], v[2:3] op_sel_hi:[1,0]
	v_pk_mul_f32 v[42:43], v[42:43], v[2:3] op_sel_hi:[1,0]
	v_pk_mul_f32 v[40:41], v[40:41], v[2:3] op_sel_hi:[1,0]
	v_pk_mul_f32 v[38:39], v[38:39], v[2:3] op_sel_hi:[1,0]
	v_pk_mul_f32 v[36:37], v[36:37], v[2:3] op_sel_hi:[1,0]
	v_pk_mul_f32 v[34:35], v[34:35], v[2:3] op_sel_hi:[1,0]
	v_pk_mul_f32 v[32:33], v[32:33], v[2:3] op_sel_hi:[1,0]
	v_pk_mul_f32 v[30:31], v[30:31], v[2:3] op_sel_hi:[1,0]
	v_pk_mul_f32 v[28:29], v[28:29], v[2:3] op_sel_hi:[1,0]
	v_pk_mul_f32 v[26:27], v[26:27], v[2:3] op_sel_hi:[1,0]
	v_pk_mul_f32 v[24:25], v[24:25], v[2:3] op_sel_hi:[1,0]
	v_pk_mul_f32 v[22:23], v[22:23], v[2:3] op_sel_hi:[1,0]
	v_pk_mul_f32 v[20:21], v[20:21], v[2:3] op_sel_hi:[1,0]
	v_pk_mul_f32 v[18:19], v[18:19], v[2:3] op_sel_hi:[1,0]

.LBB0_791:
	s_nop 0
	v_max3_f32 v2, v50, v51, v52
	v_max3_f32 v16, v53, v54, v55
	v_max3_f32 v17, v56, v57, v58
	v_max3_f32 v114, v59, v60, v61
	v_max3_f32 v2, v2, v16, v17
	v_max3_f32 v16, v62, v63, v64
	v_max3_f32 v2, v2, v114, v16
	v_max_f32_e32 v2, v2, v65
	v_sub_f32_e32 v16, v2, v113
	v_cmp_ge_f32_e32 vcc, s76, v16
	s_cmp_eq_u64 vcc, exec
	s_cbranch_scc1 .LBB0_770
	v_mov_b32_e32 v16, v2
	s_nop 1
	v_permlane32_swap_b32_e32 v2, v16
	v_max_f32_e32 v2, v2, v16
	v_max_f32_e32 v2, v2, v2
	v_max_f32_e32 v16, v113, v113
	v_max_f32_e32 v16, v16, v2
	v_sub_f32_e32 v2, v113, v16
	v_mul_f32_e32 v2, 0x3fb8aa3b, v2
	v_exp_f32_e32 v2, v2
	v_mov_b32_e32 v113, v16
	v_mul_f32_e32 v108, v108, v2
	v_pk_mul_f32 v[48:49], v[48:49], v[2:3] op_sel_hi:[1,0]
	v_pk_mul_f32 v[46:47], v[46:47], v[2:3] op_sel_hi:[1,0]
	v_pk_mul_f32 v[44:45], v[44:45], v[2:3] op_sel_hi:[1,0]
	v_pk_mul_f32 v[42:43], v[42:43], v[2:3] op_sel_hi:[1,0]
	v_pk_mul_f32 v[40:41], v[40:41], v[2:3] op_sel_hi:[1,0]
	v_pk_mul_f32 v[38:39], v[38:39], v[2:3] op_sel_hi:[1,0]
	v_pk_mul_f32 v[36:37], v[36:37], v[2:3] op_sel_hi:[1,0]
	v_pk_mul_f32 v[34:35], v[34:35], v[2:3] op_sel_hi:[1,0]
	v_pk_mul_f32 v[32:33], v[32:33], v[2:3] op_sel_hi:[1,0]
	v_pk_mul_f32 v[30:31], v[30:31], v[2:3] op_sel_hi:[1,0]
	v_pk_mul_f32 v[28:29], v[28:29], v[2:3] op_sel_hi:[1,0]
	v_pk_mul_f32 v[26:27], v[26:27], v[2:3] op_sel_hi:[1,0]
	v_pk_mul_f32 v[24:25], v[24:25], v[2:3] op_sel_hi:[1,0]
	v_pk_mul_f32 v[22:23], v[22:23], v[2:3] op_sel_hi:[1,0]
	v_pk_mul_f32 v[20:21], v[20:21], v[2:3] op_sel_hi:[1,0]
	v_pk_mul_f32 v[18:19], v[18:19], v[2:3] op_sel_hi:[1,0]
	s_branch .LBB0_770
